# attention: four more v_add / three more v_exp of the softmax tail pulled ahead of the first MFMA of each half (filling the K-fragment LDS wait); on top of v58
# speedup vs baseline: 1.0027x; 1.0027x over previous
.LBB0_1344:
	ds_read_b128 v[230:233], v203 offset:24576
	ds_read_b128 v[236:239], v203 offset:36864
	ds_read_b128 v[240:243], v204 offset:24576
	ds_read_b128 v[244:247], v204 offset:36864
	ds_read_b128 v[66:69], v201 offset:36864
	ds_read_b128 v[70:73], v201 offset:24576
	ds_read_b128 v[212:215], v202 offset:24576
	ds_read_b128 v[216:219], v202 offset:36864
	v_add_f32_e32 v168, 0, v169
	v_add_f32_e32 v168, v191, v168
	v_add_f32_e32 v168, v170, v168
	v_add_f32_e32 v168, v192, v168
	v_add_f32_e32 v168, v190, v168
	v_add_f32_e32 v168, v193, v168
	v_add_f32_e32 v168, v171, v168
	s_waitcnt lgkmcnt(2)
	v_mfma_f32_32x32x16_bf16 v[82:97], v[70:73], v[128:131], 0
	v_add_f32_e32 v168, v189, v168
	v_add_f32_e32 v168, v173, v168
	v_add_f32_e32 v168, v175, v168
	v_mfma_f32_32x32x16_bf16 v[66:81], v[66:69], v[128:131], 0
	v_add_f32_e32 v168, v174, v168
	v_add_f32_e32 v168, v188, v168
	v_exp_f32_e32 v162, v162
	v_add_f32_e32 v168, v164, v168
	v_exp_f32_e32 v163, v163
	v_add_f32_e32 v168, v166, v168
	v_exp_f32_e32 v160, v160
	v_mfma_f32_32x32x16_bf16 v[82:97], v[230:233], v[124:127], v[82:97]
	v_add_f32_e32 v168, v165, v168
	v_exp_f32_e32 v161, v161
	v_add_f32_e32 v168, v167, v168
	v_exp_f32_e32 v156, v156
	v_add_f32_e32 v168, v162, v168
	v_exp_f32_e32 v157, v157
	v_add_f32_e32 v168, v163, v168
	v_mfma_f32_32x32x16_bf16 v[66:81], v[236:239], v[124:127], v[66:81]
	ds_read_b128 v[230:233], v201 offset:24704
	ds_read_b128 v[236:239], v201 offset:36992
	v_exp_f32_e32 v152, v152
	v_add_f32_e32 v168, v160, v168
	v_exp_f32_e32 v153, v153
	v_add_f32_e32 v168, v161, v168
	v_exp_f32_e32 v150, v150
	v_add_f32_e32 v168, v156, v168
	v_mfma_f32_32x32x16_bf16 v[82:97], v[240:243], v[120:123], v[82:97]
	v_exp_f32_e32 v151, v151
	v_add_f32_e32 v168, v157, v168
	v_exp_f32_e32 v158, v158
	v_add_f32_e32 v168, v152, v168
	v_exp_f32_e32 v159, v159
	v_add_f32_e32 v168, v153, v168
	v_exp_f32_e32 v154, v154
	v_mfma_f32_32x32x16_bf16 v[66:81], v[244:247], v[120:123], v[66:81]
	ds_read_b128 v[240:243], v203 offset:24704
	ds_read_b128 v[244:247], v203 offset:36992
	v_add_f32_e32 v168, v150, v168
	v_exp_f32_e32 v155, v155
	v_add_f32_e32 v168, v151, v168
	v_exp_f32_e32 v148, v148
	v_add_f32_e32 v168, v158, v168
	v_exp_f32_e32 v149, v149
	s_waitcnt lgkmcnt(5)
	v_mfma_f32_32x32x16_bf16 v[82:97], v[212:215], v[116:119], v[82:97]
	v_add_f32_e32 v168, v159, v168
	v_add_f32_e32 v168, v154, v168
	v_add_f32_e32 v168, v155, v168
	v_add_f32_e32 v168, v148, v168
	s_waitcnt lgkmcnt(4)
	v_mfma_f32_32x32x16_bf16 v[66:81], v[216:219], v[116:119], v[66:81]
	ds_read_b128 v[212:215], v204 offset:24704
	ds_read_b128 v[216:219], v204 offset:36992
	s_waitcnt lgkmcnt(5)
	v_mfma_f32_32x32x16_bf16 v[82:97], v[230:233], v[112:115], v[82:97]
	s_waitcnt lgkmcnt(4)
	v_mfma_f32_32x32x16_bf16 v[66:81], v[236:239], v[112:115], v[66:81]
	ds_read_b128 v[230:233], v202 offset:24704
	ds_read_b128 v[236:239], v202 offset:36992
	s_waitcnt lgkmcnt(5)
	v_mfma_f32_32x32x16_bf16 v[82:97], v[240:243], v[108:111], v[82:97]
	s_waitcnt lgkmcnt(4)
	v_mfma_f32_32x32x16_bf16 v[66:81], v[244:247], v[108:111], v[66:81]
	ds_read_b128 v[240:243], v201 offset:24832
	ds_read_b128 v[244:247], v201 offset:37120
	s_waitcnt lgkmcnt(5)
	v_mfma_f32_32x32x16_bf16 v[82:97], v[212:215], v[104:107], v[82:97]
	s_waitcnt lgkmcnt(4)
	v_mfma_f32_32x32x16_bf16 v[66:81], v[216:219], v[104:107], v[66:81]
	ds_read_b128 v[212:215], v203 offset:24832
	ds_read_b128 v[216:219], v203 offset:37120
	s_waitcnt lgkmcnt(5)
	v_mfma_f32_32x32x16_bf16 v[82:97], v[230:233], v[100:103], v[82:97]
	s_waitcnt lgkmcnt(4)
	v_mfma_f32_32x32x16_bf16 v[66:81], v[236:239], v[100:103], v[66:81]
	ds_read_b128 v[230:233], v204 offset:24832
	ds_read_b128 v[236:239], v204 offset:37120
	s_waitcnt lgkmcnt(5)
	v_mfma_f32_32x32x16_bf16 v[82:97], v[240:243], v[144:147], v[82:97]
	s_waitcnt lgkmcnt(4)
	v_mfma_f32_32x32x16_bf16 v[66:81], v[244:247], v[144:147], v[66:81]
	ds_read_b128 v[240:243], v202 offset:24832
	ds_read_b128 v[244:247], v202 offset:37120
	s_waitcnt lgkmcnt(5)
	v_mfma_f32_32x32x16_bf16 v[82:97], v[212:215], v[140:143], v[82:97]
	v_add_f32_e32 v212, v149, v168
	v_mov_b32_e32 v213, v212
	v_cvt_pk_bf16_f32 v168, v169, v191
	v_cvt_pk_bf16_f32 v169, v170, v192
	v_cvt_pk_bf16_f32 v170, v190, v193
	v_cvt_pk_bf16_f32 v171, v171, v189
	v_cvt_pk_bf16_f32 v172, v173, v175
	s_waitcnt lgkmcnt(4)
	v_mfma_f32_32x32x16_bf16 v[66:81], v[216:219], v[140:143], v[66:81]
	v_cvt_pk_bf16_f32 v173, v174, v188
	v_cvt_pk_bf16_f32 v174, v164, v166
	v_permlane32_swap_b32_e32 v212, v213
	v_permlane32_swap_b32_e32 v168, v170
	v_cvt_pk_bf16_f32 v175, v165, v167
	s_waitcnt lgkmcnt(3)
	v_mfma_f32_32x32x16_bf16 v[82:97], v[230:233], v[136:139], v[82:97]
	v_permlane32_swap_b32_e32 v172, v174
	v_cvt_pk_bf16_f32 v214, v162, v163
	v_cvt_pk_bf16_f32 v215, v160, v161
	v_cvt_pk_bf16_f32 v216, v156, v157
	v_cvt_pk_bf16_f32 v217, v152, v153
	v_cvt_pk_bf16_f32 v230, v150, v151
	s_waitcnt lgkmcnt(2)
	v_mfma_f32_32x32x16_bf16 v[66:81], v[236:239], v[136:139], v[66:81]
	v_cvt_pk_bf16_f32 v231, v158, v159
	v_cvt_pk_bf16_f32 v232, v154, v155
	v_cvt_pk_bf16_f32 v233, v148, v149
	v_permlane32_swap_b32_e32 v169, v171
	v_permlane32_swap_b32_e32 v173, v175
	s_waitcnt lgkmcnt(1)
	v_mfma_f32_32x32x16_bf16 v[82:97], v[240:243], v[132:135], v[82:97]
	v_permlane32_swap_b32_e32 v214, v216
	v_permlane32_swap_b32_e32 v215, v217
	v_permlane32_swap_b32_e32 v230, v232
	v_permlane32_swap_b32_e32 v231, v233
	s_waitcnt lgkmcnt(0)
	v_mfma_f32_32x32x16_bf16 v[66:81], v[244:247], v[132:135], v[66:81]
	v_readfirstlane_b32 s4, v0
	s_nop 0
	s_lshl_b32 s5, s4, 4
	s_mul_i32 s4, s5, 3
	s_add_i32 m0, s4, 0x8000
	s_nop 0
	global_load_lds_dwordx4 v[182:183], off
	s_add_i32 m0, s4, 0x8400
	s_nop 0
	global_load_lds_dwordx4 v[184:185], off
	s_add_i32 m0, s4, 0x8800
	s_nop 0
	global_load_lds_dwordx4 v[186:187], off
	s_lshl_b32 s5, s5, 1
	s_add_i32 m0, s5, 0x4000
	s_nop 0
	global_load_lds_dwordx4 v[206:207], off
	s_add_i32 m0, s5, 0x4380
	s_nop 0
	global_load_lds_dwordx4 v[206:207], off offset:128
	v_add_co_u32_e32 v182, vcc, v182, v205
	s_nop 1
	v_addc_co_u32_e32 v183, vcc, 0, v183, vcc
	v_add_co_u32_e32 v184, vcc, v184, v208
	s_nop 1
	v_addc_co_u32_e32 v185, vcc, 0, v185, vcc
	v_add_co_u32_e32 v186, vcc, v186, v209
	s_nop 1
	v_addc_co_u32_e32 v187, vcc, 0, v187, vcc
	v_add_co_u32_e32 v206, vcc, 0x38000, v206
	s_nop 1
	v_addc_co_u32_e32 v207, vcc, 0, v207, vcc
	ds_read_b64_tr_b16 v[236:237], v200 offset:0
	ds_read_b64_tr_b16 v[238:239], v200 offset:0x800
	ds_read_b64_tr_b16 v[240:241], v200 offset:0x1000
	ds_read_b64_tr_b16 v[242:243], v200 offset:0x1800
	ds_read_b64_tr_b16 v[244:245], v200 offset:0x2000
	ds_read_b64_tr_b16 v[246:247], v200 offset:0x2800
	ds_read_b64_tr_b16 v[222:223], v200 offset:0x3000
	ds_read_b64_tr_b16 v[224:225], v200 offset:0x3800
	s_waitcnt lgkmcnt(0)
	s_nop 0
	v_mfma_f32_32x32x16_bf16 v[2:17], v[168:171], v[236:239], v[2:17]
	v_mfma_f32_32x32x16_bf16 v[2:17], v[172:175], v[240:243], v[2:17]
	v_mfma_f32_32x32x16_bf16 v[2:17], v[214:217], v[244:247], v[2:17]
	v_mfma_f32_32x32x16_bf16 v[2:17], v[230:233], v[222:225], v[2:17]
	ds_read_b64_tr_b16 v[222:223], v200 offset:0x200
	ds_read_b64_tr_b16 v[224:225], v200 offset:0xa00
	ds_read_b64_tr_b16 v[236:237], v200 offset:0x1200
	ds_read_b64_tr_b16 v[238:239], v200 offset:0x1a00
	ds_read_b64_tr_b16 v[240:241], v200 offset:0x2200
	ds_read_b64_tr_b16 v[242:243], v200 offset:0x2a00
	ds_read_b64_tr_b16 v[244:245], v200 offset:0x3200
	ds_read_b64_tr_b16 v[246:247], v200 offset:0x3a00
	s_waitcnt lgkmcnt(0)
	s_nop 0
	v_mfma_f32_32x32x16_bf16 v[50:65], v[168:171], v[222:225], v[50:65]
	ds_read_b64_tr_b16 v[222:223], v200 offset:0x400
	ds_read_b64_tr_b16 v[224:225], v200 offset:0xc00
	v_mfma_f32_32x32x16_bf16 v[50:65], v[172:175], v[236:239], v[50:65]
	ds_read_b64_tr_b16 v[236:237], v200 offset:0x1400
	ds_read_b64_tr_b16 v[238:239], v200 offset:0x1c00
	v_mfma_f32_32x32x16_bf16 v[50:65], v[214:217], v[240:243], v[50:65]
	ds_read_b64_tr_b16 v[240:241], v200 offset:0x2400
	ds_read_b64_tr_b16 v[242:243], v200 offset:0x2c00
	v_mfma_f32_32x32x16_bf16 v[50:65], v[230:233], v[244:247], v[50:65]
	ds_read_b64_tr_b16 v[244:245], v200 offset:0x3400
	ds_read_b64_tr_b16 v[246:247], v200 offset:0x3c00
	s_waitcnt lgkmcnt(0)
	v_mfma_f32_32x32x16_bf16 v[34:49], v[168:171], v[222:225], v[34:49]
	ds_read_b64_tr_b16 v[222:223], v200 offset:0x600
	ds_read_b64_tr_b16 v[224:225], v200 offset:0xe00
	v_mfma_f32_32x32x16_bf16 v[34:49], v[172:175], v[236:239], v[34:49]
	ds_read_b64_tr_b16 v[236:237], v200 offset:0x1600
	ds_read_b64_tr_b16 v[238:239], v200 offset:0x1e00
	v_mfma_f32_32x32x16_bf16 v[34:49], v[214:217], v[240:243], v[34:49]
	ds_read_b64_tr_b16 v[240:241], v200 offset:0x2600
	ds_read_b64_tr_b16 v[242:243], v200 offset:0x2e00
	v_mfma_f32_32x32x16_bf16 v[34:49], v[230:233], v[244:247], v[34:49]
	ds_read_b64_tr_b16 v[244:245], v200 offset:0x3600
	ds_read_b64_tr_b16 v[246:247], v200 offset:0x3e00
	s_waitcnt lgkmcnt(0)
	v_mfma_f32_32x32x16_bf16 v[18:33], v[168:171], v[222:225], v[18:33]
	v_max_f32_e32 v168, v83, v83
	v_max_f32_e32 v169, v82, v82
	v_max_f32_e32 v168, v169, v168
	v_max3_f32 v168, v168, v84, v85
	v_max3_f32 v168, v168, v86, v87
	v_max3_f32 v168, v168, v88, v89
	v_max3_f32 v168, v168, v90, v91
	v_max3_f32 v168, v168, v92, v93
	v_max3_f32 v168, v168, v94, v95
	v_mfma_f32_32x32x16_bf16 v[18:33], v[172:175], v[236:239], v[18:33]
	v_max3_f32 v168, v168, v96, v97
	v_max3_f32 v168, v168, v66, v67
	v_max3_f32 v168, v168, v68, v69
	v_max3_f32 v168, v168, v70, v71
	v_max3_f32 v168, v168, v72, v73
	v_max3_f32 v168, v168, v74, v75
	v_max3_f32 v168, v168, v76, v77
	v_max3_f32 v168, v168, v78, v79
	v_mfma_f32_32x32x16_bf16 v[18:33], v[214:217], v[240:243], v[18:33]
	v_max3_f32 v168, v168, v80, v81
	v_mov_b32_e32 v169, v168
	s_nop 1
	v_permlane32_swap_b32_e32 v168, v169
	v_max_f32_e32 v169, v169, v169
	v_max_f32_e32 v168, v168, v168
	v_max_f32_e32 v168, v168, v169
	v_sub_f32_e32 v169, v168, v211
	v_cmp_ge_f32_e32 vcc, s11, v169
	v_max_f32_e32 v169, v211, v211
	v_max_f32_e32 v168, v169, v168
	v_mfma_f32_32x32x16_bf16 v[18:33], v[230:233], v[244:247], v[18:33]
	v_sub_f32_e32 v169, v211, v168
	v_mul_f32_e32 v169, 0x3dd53b94, v169
	v_exp_f32_e32 v169, v169
	s_cmp_eq_u64 vcc, exec
	s_cselect_b64 s[18:19], -1, 0
	v_cndmask_b32_e64 v172, v169, 1.0, s[18:19]
	v_cmp_gt_f32_e32 vcc, 1.0, v172
	s_cbranch_vccz .LBB0_1348
	s_and_saveexec_b64 s[4:5], s[0:1]
	ds_write_b32 v197, v172 offset:128
	s_or_b64 exec, exec, s[4:5]
	s_waitcnt lgkmcnt(0)
	v_add_u32_e32 v160, v196, v98
	ds_read_b128 v[148:151], v160 offset:224
	ds_read_b128 v[152:155], v160 offset:192
	ds_read_b128 v[156:159], v160 offset:160
	ds_read_b128 v[160:163], v160 offset:128
	v_mov_b32_e32 v228, 0xffffce00
	s_waitcnt lgkmcnt(3)
	v_pk_mul_f32 v[14:15], v[14:15], v[148:149]
	s_waitcnt lgkmcnt(2)
	v_pk_mul_f32 v[10:11], v[10:11], v[152:153]
	s_waitcnt lgkmcnt(1)
	v_pk_mul_f32 v[6:7], v[6:7], v[156:157]
	v_pk_mul_f32 v[16:17], v[16:17], v[150:151]
	v_pk_mul_f32 v[12:13], v[12:13], v[154:155]
	v_pk_mul_f32 v[8:9], v[8:9], v[158:159]
	s_waitcnt lgkmcnt(0)
	v_pk_mul_f32 v[4:5], v[4:5], v[162:163]
	v_pk_mul_f32 v[2:3], v[2:3], v[160:161]
	v_pk_mul_f32 v[62:63], v[62:63], v[148:149]
	v_pk_mul_f32 v[58:59], v[58:59], v[152:153]
	v_pk_mul_f32 v[54:55], v[54:55], v[156:157]
	v_pk_mul_f32 v[64:65], v[64:65], v[150:151]
	v_pk_mul_f32 v[60:61], v[60:61], v[154:155]
	v_pk_mul_f32 v[56:57], v[56:57], v[158:159]
	v_pk_mul_f32 v[52:53], v[52:53], v[162:163]
	v_pk_mul_f32 v[50:51], v[50:51], v[160:161]
	v_pk_mul_f32 v[46:47], v[46:47], v[148:149]
	v_pk_mul_f32 v[42:43], v[42:43], v[152:153]
	v_pk_mul_f32 v[38:39], v[38:39], v[156:157]
	v_pk_mul_f32 v[48:49], v[48:49], v[150:151]
	v_pk_mul_f32 v[44:45], v[44:45], v[154:155]
	v_pk_mul_f32 v[40:41], v[40:41], v[158:159]
	v_pk_mul_f32 v[36:37], v[36:37], v[162:163]
	v_pk_mul_f32 v[34:35], v[34:35], v[160:161]
	v_pk_mul_f32 v[30:31], v[30:31], v[148:149]
	v_pk_mul_f32 v[26:27], v[26:27], v[152:153]
	v_pk_mul_f32 v[22:23], v[22:23], v[156:157]
	v_pk_mul_f32 v[32:33], v[32:33], v[150:151]
	v_pk_mul_f32 v[28:29], v[28:29], v[154:155]
	v_pk_mul_f32 v[24:25], v[24:25], v[158:159]
	v_pk_mul_f32 v[20:21], v[20:21], v[162:163]
	v_pk_mul_f32 v[18:19], v[18:19], v[160:161]
	s_branch .LBB0_1349

.LBB0_1349:
	v_cndmask_b32_e64 v173, v168, v211, s[18:19]
	v_mul_f32_e32 v164, 0xbdd53b94, v173
	v_fmamk_f32 v82, v82, 0x3dd53b94, v164
	v_fmamk_f32 v83, v83, 0x3dd53b94, v164
	v_fmamk_f32 v84, v84, 0x3dd53b94, v164
	v_fmamk_f32 v85, v85, 0x3dd53b94, v164
	v_fmamk_f32 v86, v86, 0x3dd53b94, v164
	v_fmamk_f32 v87, v87, 0x3dd53b94, v164
	v_fmamk_f32 v88, v88, 0x3dd53b94, v164
	v_fmamk_f32 v89, v89, 0x3dd53b94, v164
	v_fmamk_f32 v90, v90, 0x3dd53b94, v164
	v_fmamk_f32 v91, v91, 0x3dd53b94, v164
	v_fmamk_f32 v92, v92, 0x3dd53b94, v164
	v_fmamk_f32 v93, v93, 0x3dd53b94, v164
	v_fmamk_f32 v94, v94, 0x3dd53b94, v164
	v_fmamk_f32 v95, v95, 0x3dd53b94, v164
	v_fmamk_f32 v96, v96, 0x3dd53b94, v164
	v_fmamk_f32 v97, v97, 0x3dd53b94, v164
	v_fmamk_f32 v229, v68, 0x3dd53b94, v164
	v_fmamk_f32 v230, v69, 0x3dd53b94, v164
	v_fmamk_f32 v168, v73, 0x3dd53b94, v164
	v_fmamk_f32 v169, v74, 0x3dd53b94, v164
	v_fmamk_f32 v175, v66, 0x3dd53b94, v164
	v_fmamk_f32 v211, v67, 0x3dd53b94, v164
	v_fmamk_f32 v231, v70, 0x3dd53b94, v164
	v_fmamk_f32 v166, v71, 0x3dd53b94, v164
	v_fmamk_f32 v167, v72, 0x3dd53b94, v164
	v_fmamk_f32 v170, v75, 0x3dd53b94, v164
	v_fmamk_f32 v171, v76, 0x3dd53b94, v164
	v_fmamk_f32 v174, v77, 0x3dd53b94, v164
	v_fmamk_f32 v165, v78, 0x3dd53b94, v164
	v_exp_f32_e32 v161, v82
	v_exp_f32_e32 v163, v83
	v_exp_f32_e32 v159, v84
	v_exp_f32_e32 v162, v85
	v_exp_f32_e32 v158, v86
	v_exp_f32_e32 v160, v87
	v_exp_f32_e32 v156, v88
	v_exp_f32_e32 v157, v89
	v_exp_f32_e32 v153, v90
	v_exp_f32_e32 v155, v91
	v_exp_f32_e32 v152, v92
	v_exp_f32_e32 v154, v93
	v_exp_f32_e32 v149, v94
	v_exp_f32_e32 v151, v95
	v_exp_f32_e32 v148, v96
	v_exp_f32_e32 v150, v97
	v_fmamk_f32 v232, v79, 0x3dd53b94, v164
	v_fmamk_f32 v233, v80, 0x3dd53b94, v164
	v_fmac_f32_e32 v164, 0x3dd53b94, v81
	s_waitcnt vmcnt(0) lgkmcnt(0)
	s_barrier
	ds_read_b128 v[214:217], v203
	ds_read_b128 v[222:225], v203 offset:12288
	ds_read_b128 v[236:239], v204
	ds_read_b128 v[240:243], v204 offset:12288
	ds_read_b128 v[66:69], v201 offset:12288
	ds_read_b128 v[70:73], v201
	ds_read_b128 v[244:247], v202
	ds_read_b128 v[176:179], v202 offset:12288
	v_exp_f32_e32 v166, v166
	v_exp_f32_e32 v167, v167
	v_exp_f32_e32 v218, v169
	v_exp_f32_e32 v219, v170
	v_exp_f32_e32 v165, v165
	v_exp_f32_e32 v164, v164
	s_waitcnt lgkmcnt(2)
	v_mfma_f32_32x32x16_bf16 v[82:97], v[70:73], v[128:131], 0
	v_mfma_f32_32x32x16_bf16 v[82:97], v[214:217], v[124:127], v[82:97]
	v_mfma_f32_32x32x16_bf16 v[82:97], v[236:239], v[120:123], v[82:97]
	v_mfma_f32_32x32x16_bf16 v[66:81], v[66:69], v[128:131], 0
	s_waitcnt lgkmcnt(1)
	v_mfma_f32_32x32x16_bf16 v[82:97], v[244:247], v[116:119], v[82:97]
	v_mfma_f32_32x32x16_bf16 v[66:81], v[222:225], v[124:127], v[66:81]
	ds_read_b128 v[214:217], v201 offset:128
	ds_read_b128 v[222:225], v201 offset:12416
	s_waitcnt lgkmcnt(1)
	v_mfma_f32_32x32x16_bf16 v[82:97], v[214:217], v[112:115], v[82:97]
	v_mfma_f32_32x32x16_bf16 v[66:81], v[240:243], v[120:123], v[66:81]
	ds_read_b128 v[236:239], v203 offset:128
	ds_read_b128 v[240:243], v203 offset:12416
	s_waitcnt lgkmcnt(1)
	v_mfma_f32_32x32x16_bf16 v[82:97], v[236:239], v[108:111], v[82:97]
	v_mfma_f32_32x32x16_bf16 v[66:81], v[176:179], v[116:119], v[66:81]
	ds_read_b128 v[176:179], v204 offset:128
	ds_read_b128 v[244:247], v204 offset:12416
	s_waitcnt lgkmcnt(1)
	v_mfma_f32_32x32x16_bf16 v[82:97], v[176:179], v[104:107], v[82:97]
	v_mfma_f32_32x32x16_bf16 v[66:81], v[222:225], v[112:115], v[66:81]
	ds_read_b128 v[214:217], v202 offset:128
	ds_read_b128 v[222:225], v202 offset:12416
	s_waitcnt lgkmcnt(1)
	v_mfma_f32_32x32x16_bf16 v[82:97], v[214:217], v[100:103], v[82:97]
	v_mfma_f32_32x32x16_bf16 v[66:81], v[240:243], v[108:111], v[66:81]
	ds_read_b128 v[236:239], v201 offset:256
	ds_read_b128 v[240:243], v201 offset:12544
	s_waitcnt lgkmcnt(1)
	v_mfma_f32_32x32x16_bf16 v[82:97], v[236:239], v[144:147], v[82:97]
	v_mfma_f32_32x32x16_bf16 v[66:81], v[244:247], v[104:107], v[66:81]
	ds_read_b128 v[176:179], v203 offset:256
	ds_read_b128 v[244:247], v203 offset:12544
	s_waitcnt lgkmcnt(1)
	v_mfma_f32_32x32x16_bf16 v[82:97], v[176:179], v[140:143], v[82:97]
	v_exp_f32_e32 v178, v175
	v_exp_f32_e32 v179, v211
	v_exp_f32_e32 v211, v229
	v_mfma_f32_32x32x16_bf16 v[66:81], v[222:225], v[100:103], v[66:81]
	ds_read_b128 v[214:217], v204 offset:256
	ds_read_b128 v[222:225], v204 offset:12544
	s_waitcnt lgkmcnt(1)
	v_mfma_f32_32x32x16_bf16 v[82:97], v[214:217], v[136:139], v[82:97]
	v_exp_f32_e32 v217, v168
	v_add_f32_e32 v168, 0, v161
	v_add_f32_e32 v168, v163, v168
	v_add_f32_e32 v168, v159, v168
	v_add_f32_e32 v168, v162, v168
	v_add_f32_e32 v168, v158, v168
	v_add_f32_e32 v168, v160, v168
	v_mfma_f32_32x32x16_bf16 v[66:81], v[240:243], v[144:147], v[66:81]
	v_add_f32_e32 v168, v156, v168
	v_add_f32_e32 v168, v157, v168
	v_add_f32_e32 v168, v153, v168
	v_add_f32_e32 v168, v155, v168
	v_add_f32_e32 v168, v152, v168
	v_add_f32_e32 v168, v154, v168
	v_add_f32_e32 v168, v149, v168
	v_mfma_f32_32x32x16_bf16 v[66:81], v[244:247], v[140:143], v[66:81]
	v_add_f32_e32 v168, v151, v168
	v_add_f32_e32 v168, v148, v168
	v_exp_f32_e32 v215, v230
	v_add_f32_e32 v168, v150, v168
	v_exp_f32_e32 v216, v231
	v_add_f32_e32 v168, v178, v168
	v_add_f32_e32 v168, v179, v168
	s_waitcnt lgkmcnt(0)
	v_mfma_f32_32x32x16_bf16 v[66:81], v[222:225], v[136:139], v[66:81]
	v_add_f32_e32 v168, v211, v168
	v_add_f32_e32 v168, v215, v168
	v_add_f32_e32 v168, v216, v168
	ds_read_b128 v[236:239], v202 offset:256
	ds_read_b128 v[240:243], v202 offset:12544
	v_add_f32_e32 v168, v166, v168
	v_exp_f32_e32 v223, v171
	v_add_f32_e32 v168, v167, v168
	v_exp_f32_e32 v224, v174
	v_add_f32_e32 v168, v217, v168
	v_add_f32_e32 v168, v218, v168
	v_exp_f32_e32 v225, v232
	v_add_f32_e32 v168, v219, v168
	s_waitcnt lgkmcnt(1)
	v_mfma_f32_32x32x16_bf16 v[82:97], v[236:239], v[132:135], v[82:97]
	v_exp_f32_e32 v231, v233
	v_add_f32_e32 v168, v223, v168
	v_add_f32_e32 v168, v224, v168
	v_add_f32_e32 v168, v165, v168
	v_add_f32_e32 v168, v225, v168
	v_add_f32_e32 v168, v231, v168
	v_add_f32_e32 v229, v164, v168
	s_waitcnt lgkmcnt(0)
	v_mfma_f32_32x32x16_bf16 v[66:81], v[240:243], v[132:135], v[66:81]
	v_mov_b32_e32 v230, v229
	v_cvt_pk_bf16_f32 v168, v161, v163
	v_cvt_pk_bf16_f32 v169, v159, v162
	v_cvt_pk_bf16_f32 v170, v158, v160
	v_cvt_pk_bf16_f32 v171, v156, v157
	s_nop 1
	v_permlane32_swap_b32_e32 v229, v230
	v_permlane32_swap_b32_e32 v168, v170
	v_permlane32_swap_b32_e32 v169, v171
	v_cvt_pk_bf16_f32 v174, v153, v155
	v_cvt_pk_bf16_f32 v175, v152, v154
	v_cvt_pk_bf16_f32 v176, v149, v151
	v_cvt_pk_bf16_f32 v177, v148, v150
	v_cvt_pk_bf16_f32 v214, v178, v179
	v_cvt_pk_bf16_f32 v215, v211, v215
	v_cvt_pk_bf16_f32 v216, v216, v166
	v_cvt_pk_bf16_f32 v217, v167, v217
	v_cvt_pk_bf16_f32 v222, v218, v219
	v_cvt_pk_bf16_f32 v223, v223, v224
	v_cvt_pk_bf16_f32 v224, v165, v225
	v_cvt_pk_bf16_f32 v225, v231, v164
	s_nop 0
	v_permlane32_swap_b32_e32 v174, v176
	v_permlane32_swap_b32_e32 v175, v177
	v_permlane32_swap_b32_e32 v214, v216
	v_permlane32_swap_b32_e32 v215, v217
	v_permlane32_swap_b32_e32 v222, v224
	v_permlane32_swap_b32_e32 v223, v225
	v_readfirstlane_b32 s4, v0
	s_nop 0
	s_lshl_b32 s5, s4, 4
	s_mul_i32 s4, s5, 3
	s_add_i32 m0, s4, 0xe000
	s_nop 0
	global_load_lds_dwordx4 v[182:183], off
	s_add_i32 m0, s4, 0xe400
	s_nop 0
	global_load_lds_dwordx4 v[184:185], off
	s_add_i32 m0, s4, 0xe800
	s_nop 0
	global_load_lds_dwordx4 v[186:187], off
	s_lshl_b32 s5, s5, 1
	s_mov_b32 m0, s5
	s_nop 0
	global_load_lds_dwordx4 v[206:207], off
	s_add_i32 m0, s5, 0x380
	s_nop 0
	global_load_lds_dwordx4 v[206:207], off offset:128
	v_add_co_u32_e32 v182, vcc, v182, v205
	s_nop 1
	v_addc_co_u32_e32 v183, vcc, 0, v183, vcc
	v_add_co_u32_e32 v184, vcc, v184, v208
	s_nop 1
	v_addc_co_u32_e32 v185, vcc, 0, v185, vcc
	v_add_co_u32_e32 v186, vcc, v186, v209
	s_nop 1
	v_addc_co_u32_e32 v187, vcc, 0, v187, vcc
	v_add_co_u32_e32 v206, vcc, 0x38000, v206
	s_nop 1
	v_addc_co_u32_e32 v207, vcc, 0, v207, vcc
	ds_read_b64_tr_b16 v[188:189], v198 offset:0
	ds_read_b64_tr_b16 v[190:191], v198 offset:0x800
	ds_read_b64_tr_b16 v[236:237], v198 offset:0x1000
	ds_read_b64_tr_b16 v[238:239], v198 offset:0x1800
	ds_read_b64_tr_b16 v[240:241], v198 offset:0x2000
	ds_read_b64_tr_b16 v[242:243], v198 offset:0x2800
	ds_read_b64_tr_b16 v[244:245], v198 offset:0x3000
	ds_read_b64_tr_b16 v[246:247], v198 offset:0x3800
	s_waitcnt lgkmcnt(0)
	s_nop 0
	v_mfma_f32_32x32x16_bf16 v[2:17], v[168:171], v[188:191], v[2:17]
	ds_read_b64_tr_b16 v[188:189], v198 offset:0x200
	ds_read_b64_tr_b16 v[190:191], v198 offset:0xa00
	v_mfma_f32_32x32x16_bf16 v[2:17], v[174:177], v[236:239], v[2:17]
	ds_read_b64_tr_b16 v[236:237], v198 offset:0x1200
	ds_read_b64_tr_b16 v[238:239], v198 offset:0x1a00
	v_mfma_f32_32x32x16_bf16 v[2:17], v[214:217], v[240:243], v[2:17]
	ds_read_b64_tr_b16 v[240:241], v198 offset:0x2200
	ds_read_b64_tr_b16 v[242:243], v198 offset:0x2a00
	v_mfma_f32_32x32x16_bf16 v[2:17], v[222:225], v[244:247], v[2:17]
	ds_read_b64_tr_b16 v[244:245], v198 offset:0x3200
	ds_read_b64_tr_b16 v[246:247], v198 offset:0x3a00
	s_waitcnt lgkmcnt(0)
	v_mfma_f32_32x32x16_bf16 v[50:65], v[168:171], v[188:191], v[50:65]
	ds_read_b64_tr_b16 v[188:189], v198 offset:0x400
	ds_read_b64_tr_b16 v[190:191], v198 offset:0xc00
	v_mfma_f32_32x32x16_bf16 v[50:65], v[174:177], v[236:239], v[50:65]
	ds_read_b64_tr_b16 v[236:237], v198 offset:0x1400
	ds_read_b64_tr_b16 v[238:239], v198 offset:0x1c00
	v_mfma_f32_32x32x16_bf16 v[50:65], v[214:217], v[240:243], v[50:65]
	ds_read_b64_tr_b16 v[240:241], v198 offset:0x2400
	ds_read_b64_tr_b16 v[242:243], v198 offset:0x2c00
	v_mfma_f32_32x32x16_bf16 v[50:65], v[222:225], v[244:247], v[50:65]
	ds_read_b64_tr_b16 v[244:245], v198 offset:0x3400
	ds_read_b64_tr_b16 v[246:247], v198 offset:0x3c00
	s_waitcnt lgkmcnt(0)
	v_mfma_f32_32x32x16_bf16 v[34:49], v[168:171], v[188:191], v[34:49]
	ds_read_b64_tr_b16 v[188:189], v198 offset:0x600
	ds_read_b64_tr_b16 v[190:191], v198 offset:0xe00
	v_mfma_f32_32x32x16_bf16 v[34:49], v[174:177], v[236:239], v[34:49]
	ds_read_b64_tr_b16 v[236:237], v198 offset:0x1600
	ds_read_b64_tr_b16 v[238:239], v198 offset:0x1e00
	v_mfma_f32_32x32x16_bf16 v[34:49], v[214:217], v[240:243], v[34:49]
	ds_read_b64_tr_b16 v[240:241], v198 offset:0x2600
	ds_read_b64_tr_b16 v[242:243], v198 offset:0x2e00
	v_mfma_f32_32x32x16_bf16 v[34:49], v[222:225], v[244:247], v[34:49]
	ds_read_b64_tr_b16 v[244:245], v198 offset:0x3600
	ds_read_b64_tr_b16 v[246:247], v198 offset:0x3e00
	s_waitcnt lgkmcnt(0)
	v_mfma_f32_32x32x16_bf16 v[18:33], v[168:171], v[188:191], v[18:33]
	v_max_f32_e32 v168, v83, v83
	v_max_f32_e32 v169, v82, v82
	v_max_f32_e32 v168, v169, v168
	v_max3_f32 v168, v168, v84, v85
	v_max3_f32 v168, v168, v86, v87
	v_max3_f32 v168, v168, v88, v89
	v_max3_f32 v168, v168, v90, v91
	v_max3_f32 v168, v168, v92, v93
	v_max3_f32 v168, v168, v94, v95
	v_mfma_f32_32x32x16_bf16 v[18:33], v[174:177], v[236:239], v[18:33]
	v_max3_f32 v168, v168, v96, v97
	v_max3_f32 v168, v168, v66, v67
	v_max3_f32 v168, v168, v68, v69
	v_max3_f32 v168, v168, v70, v71
	v_max3_f32 v168, v168, v72, v73
	v_max3_f32 v168, v168, v74, v75
	v_max3_f32 v168, v168, v76, v77
	v_max3_f32 v168, v168, v78, v79
	v_mfma_f32_32x32x16_bf16 v[18:33], v[214:217], v[240:243], v[18:33]
	v_max3_f32 v168, v168, v80, v81
	v_mov_b32_e32 v169, v168
	s_nop 1
	v_permlane32_swap_b32_e32 v168, v169
	v_max_f32_e32 v169, v169, v169
	v_max_f32_e32 v168, v168, v168
	v_max_f32_e32 v168, v168, v169
	v_sub_f32_e32 v169, v168, v173
	v_cmp_ge_f32_e32 vcc, s11, v169
	v_max_f32_e32 v169, v173, v173
	v_max_f32_e32 v169, v169, v168
	v_mfma_f32_32x32x16_bf16 v[18:33], v[222:225], v[244:247], v[18:33]
	v_sub_f32_e32 v168, v173, v169
	v_mul_f32_e32 v168, 0x3dd53b94, v168
	v_exp_f32_e32 v168, v168
	s_cmp_eq_u64 vcc, exec
	s_cselect_b64 s[18:19], -1, 0
	v_cndmask_b32_e64 v168, v168, 1.0, s[18:19]
	v_cmp_gt_f32_e32 vcc, 1.0, v168
	s_cbranch_vccz .LBB0_1353
	s_mov_b64 s[4:5], exec
	s_and_b64 s[22:23], s[4:5], s[0:1]
	v_mov_b32_e32 v246, v227
	s_mov_b64 exec, s[22:23]
	ds_write_b32 v197, v168 offset:128
	s_or_b64 exec, exec, s[4:5]
	s_waitcnt lgkmcnt(0)
	v_add_u32_e32 v160, v196, v98
	ds_read_b128 v[148:151], v160 offset:224
	ds_read_b128 v[152:155], v160 offset:192
	ds_read_b128 v[156:159], v160 offset:160
	ds_read_b128 v[160:163], v160 offset:128
	s_waitcnt lgkmcnt(3)
	v_pk_mul_f32 v[14:15], v[14:15], v[148:149]
	s_waitcnt lgkmcnt(2)
	v_pk_mul_f32 v[10:11], v[10:11], v[152:153]
	s_waitcnt lgkmcnt(1)
	v_pk_mul_f32 v[6:7], v[6:7], v[156:157]
	v_pk_mul_f32 v[16:17], v[16:17], v[150:151]
	v_pk_mul_f32 v[12:13], v[12:13], v[154:155]
	v_pk_mul_f32 v[8:9], v[8:9], v[158:159]
	s_waitcnt lgkmcnt(0)
	v_pk_mul_f32 v[4:5], v[4:5], v[162:163]
	v_pk_mul_f32 v[2:3], v[2:3], v[160:161]
	v_pk_mul_f32 v[62:63], v[62:63], v[148:149]
	v_pk_mul_f32 v[58:59], v[58:59], v[152:153]
	v_pk_mul_f32 v[54:55], v[54:55], v[156:157]
	v_pk_mul_f32 v[64:65], v[64:65], v[150:151]
	v_pk_mul_f32 v[60:61], v[60:61], v[154:155]
	v_pk_mul_f32 v[56:57], v[56:57], v[158:159]
	v_pk_mul_f32 v[52:53], v[52:53], v[162:163]
	v_pk_mul_f32 v[50:51], v[50:51], v[160:161]
	v_pk_mul_f32 v[46:47], v[46:47], v[148:149]
	v_pk_mul_f32 v[42:43], v[42:43], v[152:153]
	v_pk_mul_f32 v[38:39], v[38:39], v[156:157]
	v_pk_mul_f32 v[48:49], v[48:49], v[150:151]
	v_pk_mul_f32 v[44:45], v[44:45], v[154:155]
	v_pk_mul_f32 v[40:41], v[40:41], v[158:159]
	v_pk_mul_f32 v[36:37], v[36:37], v[162:163]
	v_pk_mul_f32 v[34:35], v[34:35], v[160:161]
	v_pk_mul_f32 v[30:31], v[30:31], v[148:149]
	v_pk_mul_f32 v[26:27], v[26:27], v[152:153]
	v_pk_mul_f32 v[22:23], v[22:23], v[156:157]
	v_pk_mul_f32 v[32:33], v[32:33], v[150:151]
	v_pk_mul_f32 v[28:29], v[28:29], v[154:155]
	v_pk_mul_f32 v[24:25], v[24:25], v[158:159]
	v_pk_mul_f32 v[20:21], v[20:21], v[162:163]
	v_pk_mul_f32 v[18:19], v[18:19], v[160:161]
	s_branch .LBB0_1354
